# P4: 7/16 of the workgroups (instead of 3/8) run the expert-weight conversion first
# baseline (speedup 1.0000x reference)
; #define LAS __attribute__((address_space(3)))
; __device__ __forceinline__ void attn_queues(const P& p, LAS unsigned char* lds, int* ctr, const int xg) {
;     ...
;     const int tid = threadIdx.x, nq = xg >= 0 ? 4 * 16 : NB * 8 * 16;
;     int* c0 = ctr + (xg >= 0 ? xg : 0); int* c1 = ctr + 64 + (xg >= 0 ? xg : 0);
;     {   if (tid == 0) qs[0] = atomicAdd(c0, 1);
; __device__ __forceinline__ void phase_attn(const P& p, LAS unsigned char* lds, int G, int bid) {
;     int* ctr = (int*)(p.ws + WS_CTL + 61440); const int xg = (G == 256) ? (bid & 7) : -1;
;     if (MOE_FP8 && ((bid >> 3) & 7) < 3) { conv_queue(p, lds, ctr + 128, -1); attn_queues(p, lds, ctr, xg); }
;     else { attn_queues(p, lds, ctr, xg); if (MOE_FP8) conv_queue(p, lds, ctr + 128, -1); }
.LBB0_688:
	s_cmp_lt_i32 s88, 5
	s_cselect_b64 s[2:3], -1, 0
	s_and_b64 s[0:1], s[2:3], s[0:1]
	s_andn2_b64 vcc, exec, s[0:1]
	v_writelane_b32 v242, s76, 35
	s_cbranch_vccnz .LBB0_924
	s_add_u32 s0, s74, 0xf000
	v_writelane_b32 v242, s0, 36
	s_addc_u32 s0, s75, 0
	s_cmpk_lg_i32 s76, 0x100
	v_writelane_b32 v242, s0, 37
	s_cselect_b64 s[0:1], -1, 0
	s_and_b32 s4, s70, 7
	v_writelane_b32 v242, s0, 38
	s_cmpk_eq_i32 s76, 0x100
	s_nop 0
	v_writelane_b32 v242, s1, 39
	s_cselect_b64 s[0:1], -1, 0
	v_writelane_b32 v242, s0, 40
	s_nop 1
	v_writelane_b32 v242, s1, 41
	s_and_b64 s[0:1], s[0:1], exec
	v_writelane_b32 v242, s4, 42
	s_cselect_b32 s0, s4, -1
	v_writelane_b32 v242, s0, 43
	s_and_b32 s0, s70, 0x78
	s_cmp_gt_u32 s0, 55
	s_mov_b64 s[0:1], -1
	v_writelane_b32 v242, s2, 44
	s_nop 1
	v_writelane_b32 v242, s3, 45
	s_cbranch_scc0 .LBB0_806
	v_readlane_b32 s0, v242, 40
	v_readlane_b32 s1, v242, 41
	s_and_b64 s[0:1], s[0:1], exec
	v_readlane_b32 s0, v242, 42
	s_cselect_b32 s0, s0, 0
	s_lshl_b32 s33, s0, 2
	v_readlane_b32 s0, v242, 36
	s_add_u32 s70, s0, s33
	v_readlane_b32 s0, v242, 37
	s_addc_u32 s71, s0, 0
	s_mov_b64 s[0:1], exec
	v_readlane_b32 s2, v242, 31
	v_readlane_b32 s3, v242, 32
	s_and_b64 s[2:3], s[0:1], s[2:3]
	s_mov_b64 exec, s[2:3]
	s_cbranch_execz .LBB0_694
	s_mov_b64 s[6:7], exec
	v_mbcnt_lo_u32_b32 v1, s6, 0
	v_mbcnt_hi_u32_b32 v1, s7, v1
	v_cmp_eq_u32_e32 vcc, 0, v1
	s_and_saveexec_b64 s[4:5], vcc
	s_cbranch_execz .LBB0_693
	s_bcnt1_i32_b64 s2, s[6:7]
	s_waitcnt vmcnt(3)
	v_mov_b32_e32 v2, 0
	v_mov_b32_e32 v3, s2
	global_atomic_add v2, v2, v3, s[70:71] sc0
